# speedup vs baseline: 1.0101x; 1.0017x over previous
.Lk1_nowarm9:
	buffer_load_dword v8, v1, s[8:11], s40 offen nt
	buffer_load_dword v9, v1, s[8:11], s41 offen nt
	buffer_load_dword v10, v1, s[8:11], s42 offen nt
	buffer_load_dword v11, v1, s[8:11], s43 offen nt
	buffer_load_dword v12, v1, s[8:11], s44 offen nt
	buffer_load_dword v13, v1, s[8:11], s45 offen nt
	buffer_load_dword v14, v1, s[8:11], s46 offen nt
	buffer_load_dword v15, v1, s[8:11], s47 offen nt
	buffer_load_dword v16, v1, s[8:11], s48 offen nt
	buffer_load_dword v17, v1, s[8:11], s49 offen nt
	buffer_load_dword v18, v1, s[8:11], s50 offen nt
	buffer_load_dword v19, v1, s[8:11], s51 offen nt
	buffer_load_dword v20, v1, s[8:11], s52 offen nt
	buffer_load_dword v21, v1, s[8:11], s53 offen nt
	buffer_load_dword v22, v1, s[8:11], s54 offen nt
	buffer_load_dword v23, v1, s[8:11], s55 offen nt
	s_add_u32 s8, s8, 0x4e200
	s_addc_u32 s9, s9, 0
	buffer_load_dword v24, v1, s[8:11], s40 offen nt
	buffer_load_dword v25, v1, s[8:11], s41 offen nt
	buffer_load_dword v26, v1, s[8:11], s42 offen nt
	buffer_load_dword v27, v1, s[8:11], s43 offen nt
	buffer_load_dword v28, v1, s[8:11], s44 offen nt
	buffer_load_dword v29, v1, s[8:11], s45 offen nt
	buffer_load_dword v30, v1, s[8:11], s46 offen nt
	buffer_load_dword v31, v1, s[8:11], s47 offen nt
	buffer_load_dword v32, v1, s[8:11], s48 offen nt
	buffer_load_dword v33, v1, s[8:11], s49 offen nt
	buffer_load_dword v34, v1, s[8:11], s50 offen nt
	buffer_load_dword v35, v1, s[8:11], s51 offen nt
	buffer_load_dword v36, v1, s[8:11], s52 offen nt
	buffer_load_dword v37, v1, s[8:11], s53 offen nt
	buffer_load_dword v38, v1, s[8:11], s54 offen nt
	buffer_load_dword v39, v1, s[8:11], s55 offen nt
	s_add_u32 s8, s8, 0x4e200
	s_addc_u32 s9, s9, 0
	buffer_load_dword v40, v1, s[8:11], s40 offen nt
	buffer_load_dword v41, v1, s[8:11], s41 offen nt
	buffer_load_dword v42, v1, s[8:11], s42 offen nt
	buffer_load_dword v43, v1, s[8:11], s43 offen nt
	buffer_load_dword v44, v1, s[8:11], s44 offen nt
	buffer_load_dword v45, v1, s[8:11], s45 offen nt
	buffer_load_dword v46, v1, s[8:11], s46 offen nt
	buffer_load_dword v47, v1, s[8:11], s47 offen nt
	buffer_load_dword v48, v1, s[8:11], s48 offen nt
	buffer_load_dword v49, v1, s[8:11], s49 offen nt
	buffer_load_dword v50, v1, s[8:11], s50 offen nt
	buffer_load_dword v51, v1, s[8:11], s51 offen nt
	buffer_load_dword v52, v1, s[8:11], s52 offen nt
	buffer_load_dword v53, v1, s[8:11], s53 offen nt
	buffer_load_dword v54, v1, s[8:11], s54 offen nt
	buffer_load_dword v55, v1, s[8:11], s55 offen nt
	v_mul_u32_u24_e32 v3, 0x147b, v2
	v_lshrrev_b32_e32 v3, 19, v3
	v_mul_u32_u24_e32 v98, 0x64, v3
	v_sub_u32_e32 v98, v2, v98
	v_add_u32_e32 v3, -1, v3
	v_add_u32_e32 v98, -1, v98
	s_movk_i32 s17, 0x62
	v_cmp_gt_u32_e64 s[36:37], 48, v3
	v_cmp_gt_u32_e64 s[38:39], s17, v98
	s_mul_i32 s17, s15, 0x1388
	v_add_lshl_u32 v98, v2, s17, 3
	s_and_b64 s[36:37], s[36:37], s[38:39]
	s_waitcnt vmcnt(32)
	s_add_u32 s8, s8, 0x4e200
	s_addc_u32 s9, s9, 0
	buffer_load_dword v56, v1, s[8:11], s40 offen nt
	buffer_load_dword v57, v1, s[8:11], s41 offen nt
	buffer_load_dword v58, v1, s[8:11], s42 offen nt
	buffer_load_dword v59, v1, s[8:11], s43 offen nt
	buffer_load_dword v60, v1, s[8:11], s44 offen nt
	buffer_load_dword v61, v1, s[8:11], s45 offen nt
	buffer_load_dword v62, v1, s[8:11], s46 offen nt
	buffer_load_dword v63, v1, s[8:11], s47 offen nt
	buffer_load_dword v64, v1, s[8:11], s48 offen nt
	buffer_load_dword v65, v1, s[8:11], s49 offen nt
	buffer_load_dword v66, v1, s[8:11], s50 offen nt
	buffer_load_dword v67, v1, s[8:11], s51 offen nt
	buffer_load_dword v68, v1, s[8:11], s52 offen nt
	buffer_load_dword v69, v1, s[8:11], s53 offen nt
	buffer_load_dword v70, v1, s[8:11], s54 offen nt
	buffer_load_dword v71, v1, s[8:11], s55 offen nt
	s_add_u32 s8, s8, 0x4e200
	s_addc_u32 s9, s9, 0
	buffer_load_dword v72, v1, s[8:11], s40 offen nt
	v_max3_f32 v76, v8, v9, v10
	v_max3_f32 v76, v76, v11, v12
	v_max3_f32 v76, v76, v13, v14
	v_max3_f32 v76, v76, v15, v16
	v_max3_f32 v76, v76, v17, v18
	v_max3_f32 v76, v76, v19, v20
	v_max3_f32 v76, v76, v21, v22
	v_max_f32_e32 v76, v76, v23
	v_sub_f32_e32 v8, v8, v76
	v_sub_f32_e32 v9, v9, v76
	v_sub_f32_e32 v10, v10, v76
	v_sub_f32_e32 v11, v11, v76
	v_sub_f32_e32 v12, v12, v76
	v_sub_f32_e32 v13, v13, v76
	v_sub_f32_e32 v14, v14, v76
	v_sub_f32_e32 v15, v15, v76
	v_sub_f32_e32 v16, v16, v76
	v_sub_f32_e32 v17, v17, v76
	v_sub_f32_e32 v18, v18, v76
	v_sub_f32_e32 v19, v19, v76
	v_sub_f32_e32 v20, v20, v76
	v_sub_f32_e32 v21, v21, v76
	v_sub_f32_e32 v22, v22, v76
	v_sub_f32_e32 v23, v23, v76
	v_or_b32_e32 v81, 0, v8
	v_or_b32_e32 v82, 1, v9
	v_min_u32_e32 v80, v81, v82
	v_or_b32_e32 v81, 2, v10
	v_or_b32_e32 v82, 3, v11
	v_min3_u32 v80, v80, v81, v82
	v_or_b32_e32 v81, 4, v12
	v_or_b32_e32 v82, 5, v13
	v_min3_u32 v80, v80, v81, v82
	v_or_b32_e32 v81, 6, v14
	v_or_b32_e32 v82, 7, v15
	v_min3_u32 v80, v80, v81, v82
	v_or_b32_e32 v81, 8, v16
	v_or_b32_e32 v82, 9, v17
	v_min3_u32 v80, v80, v81, v82
	v_or_b32_e32 v81, 10, v18
	v_or_b32_e32 v82, 11, v19
	v_min3_u32 v80, v80, v81, v82
	v_or_b32_e32 v81, 12, v20
	v_or_b32_e32 v82, 13, v21
	v_min3_u32 v80, v80, v81, v82
	v_or_b32_e32 v81, 14, v22
	v_or_b32_e32 v82, 15, v23
	v_min3_u32 v80, v80, v81, v82
	v_mul_f32_e32 v8, s14, v8
	v_mul_f32_e32 v9, s14, v9
	v_mul_f32_e32 v10, s14, v10
	v_mul_f32_e32 v11, s14, v11
	v_mul_f32_e32 v12, s14, v12
	v_mul_f32_e32 v13, s14, v13
	v_mul_f32_e32 v14, s14, v14
	v_mul_f32_e32 v15, s14, v15
	v_mul_f32_e32 v16, s14, v16
	v_mul_f32_e32 v17, s14, v17
	v_mul_f32_e32 v18, s14, v18
	v_mul_f32_e32 v19, s14, v19
	v_mul_f32_e32 v20, s14, v20
	v_mul_f32_e32 v21, s14, v21
	v_mul_f32_e32 v22, s14, v22
	v_mul_f32_e32 v23, s14, v23
	v_exp_f32_e32 v8, v8
	v_exp_f32_e32 v9, v9
	v_exp_f32_e32 v10, v10
	v_exp_f32_e32 v11, v11
	v_exp_f32_e32 v12, v12
	v_exp_f32_e32 v13, v13
	v_exp_f32_e32 v14, v14
	v_exp_f32_e32 v15, v15
	v_exp_f32_e32 v16, v16
	v_exp_f32_e32 v17, v17
	v_exp_f32_e32 v18, v18
	v_exp_f32_e32 v19, v19
	v_exp_f32_e32 v20, v20
	v_exp_f32_e32 v21, v21
	v_exp_f32_e32 v22, v22
	v_exp_f32_e32 v23, v23
	v_add_f32_e32 v78, v8, v10
	v_add_f32_e32 v79, v9, v11
	v_add_f32_e32 v78, v78, v12
	v_add_f32_e32 v79, v79, v13
	v_add_f32_e32 v78, v78, v14
	v_add_f32_e32 v79, v79, v15
	v_add_f32_e32 v78, v78, v16
	v_add_f32_e32 v79, v79, v17
	v_add_f32_e32 v78, v78, v18
	v_add_f32_e32 v79, v79, v19
	v_add_f32_e32 v78, v78, v20
	v_add_f32_e32 v79, v79, v21
	v_add_f32_e32 v78, v78, v22
	v_add_f32_e32 v79, v79, v23
	v_add_f32_e32 v78, v78, v79
	v_cvt_f64_f32_e32 v[86:87], v78
	v_mov_b32_e32 v75, v80
	v_mov_b32_e32 v73, v76
	s_waitcnt vmcnt(33)
	v_max3_f32 v76, v24, v25, v26
	v_max3_f32 v76, v76, v27, v28
	v_max3_f32 v76, v76, v29, v30
	v_max3_f32 v76, v76, v31, v32
	v_max3_f32 v76, v76, v33, v34
	v_max3_f32 v76, v76, v35, v36
	v_max3_f32 v76, v76, v37, v38
	v_max_f32_e32 v76, v76, v39
	v_max_f32_e32 v77, v73, v76
	v_cmp_gt_f32_e64 s[20:21], v76, v73
	v_sub_f32_e32 v83, v73, v77
	v_mul_f32_e32 v83, s14, v83
	v_exp_f32_e32 v83, v83
	v_sub_f32_e32 v24, v24, v77
	v_sub_f32_e32 v25, v25, v77
	v_sub_f32_e32 v26, v26, v77
	v_sub_f32_e32 v27, v27, v77
	v_sub_f32_e32 v28, v28, v77
	v_sub_f32_e32 v29, v29, v77
	v_sub_f32_e32 v30, v30, v77
	v_sub_f32_e32 v31, v31, v77
	v_sub_f32_e32 v32, v32, v77
	v_sub_f32_e32 v33, v33, v77
	v_sub_f32_e32 v34, v34, v77
	v_sub_f32_e32 v35, v35, v77
	v_sub_f32_e32 v36, v36, v77
	v_sub_f32_e32 v37, v37, v77
	v_sub_f32_e32 v38, v38, v77
	v_sub_f32_e32 v39, v39, v77
	v_cvt_f64_f32_e32 v[84:85], v83
	v_or_b32_e32 v81, 16, v24
	v_or_b32_e32 v82, 17, v25
	v_min_u32_e32 v80, v81, v82
	v_or_b32_e32 v81, 18, v26
	v_or_b32_e32 v82, 19, v27
	v_min3_u32 v80, v80, v81, v82
	v_or_b32_e32 v81, 20, v28
	v_or_b32_e32 v82, 21, v29
	v_min3_u32 v80, v80, v81, v82
	v_or_b32_e32 v81, 22, v30
	v_or_b32_e32 v82, 23, v31
	v_min3_u32 v80, v80, v81, v82
	v_or_b32_e32 v81, 24, v32
	v_or_b32_e32 v82, 25, v33
	v_min3_u32 v80, v80, v81, v82
	v_or_b32_e32 v81, 26, v34
	v_or_b32_e32 v82, 27, v35
	v_min3_u32 v80, v80, v81, v82
	v_or_b32_e32 v81, 28, v36
	v_or_b32_e32 v82, 29, v37
	v_min3_u32 v80, v80, v81, v82
	v_or_b32_e32 v81, 30, v38
	v_or_b32_e32 v82, 31, v39
	v_min3_u32 v80, v80, v81, v82
	v_mul_f64 v[86:87], v[86:87], v[84:85]
	v_mul_f32_e32 v24, s14, v24
	v_mul_f32_e32 v25, s14, v25
	v_mul_f32_e32 v26, s14, v26
	v_mul_f32_e32 v27, s14, v27
	v_mul_f32_e32 v28, s14, v28
	v_mul_f32_e32 v29, s14, v29
	v_mul_f32_e32 v30, s14, v30
	v_mul_f32_e32 v31, s14, v31
	v_mul_f32_e32 v32, s14, v32
	v_mul_f32_e32 v33, s14, v33
	v_mul_f32_e32 v34, s14, v34
	v_mul_f32_e32 v35, s14, v35
	v_mul_f32_e32 v36, s14, v36
	v_mul_f32_e32 v37, s14, v37
	v_mul_f32_e32 v38, s14, v38
	v_mul_f32_e32 v39, s14, v39
	v_exp_f32_e32 v24, v24
	v_exp_f32_e32 v25, v25
	v_exp_f32_e32 v26, v26
	v_exp_f32_e32 v27, v27
	v_exp_f32_e32 v28, v28
	v_exp_f32_e32 v29, v29
	v_exp_f32_e32 v30, v30
	v_exp_f32_e32 v31, v31
	v_exp_f32_e32 v32, v32
	v_exp_f32_e32 v33, v33
	v_exp_f32_e32 v34, v34
	v_exp_f32_e32 v35, v35
	v_exp_f32_e32 v36, v36
	v_exp_f32_e32 v37, v37
	v_exp_f32_e32 v38, v38
	v_exp_f32_e32 v39, v39
	v_add_f32_e32 v78, v24, v26
	v_add_f32_e32 v79, v25, v27
	v_add_f32_e32 v78, v78, v28
	v_add_f32_e32 v79, v79, v29
	v_add_f32_e32 v78, v78, v30
	v_add_f32_e32 v79, v79, v31
	v_add_f32_e32 v78, v78, v32
	v_add_f32_e32 v79, v79, v33
	v_add_f32_e32 v78, v78, v34
	v_add_f32_e32 v79, v79, v35
	v_add_f32_e32 v78, v78, v36
	v_add_f32_e32 v79, v79, v37
	v_add_f32_e32 v78, v78, v38
	v_add_f32_e32 v79, v79, v39
	v_add_f32_e32 v78, v78, v79
	v_cvt_f64_f32_e32 v[84:85], v78
	v_cndmask_b32_e64 v75, v75, v80, s[20:21]
	v_mov_b32_e32 v73, v77
	v_add_f64 v[86:87], v[86:87], v[84:85]
	s_waitcnt vmcnt(17)
	v_max3_f32 v76, v40, v41, v42
	v_max3_f32 v76, v76, v43, v44
	v_max3_f32 v76, v76, v45, v46
	v_max3_f32 v76, v76, v47, v48
	v_max3_f32 v76, v76, v49, v50
	v_max3_f32 v76, v76, v51, v52
	v_max3_f32 v76, v76, v53, v54
	v_max_f32_e32 v76, v76, v55
	v_max_f32_e32 v77, v73, v76
	v_cmp_gt_f32_e64 s[20:21], v76, v73
	v_sub_f32_e32 v83, v73, v77
	v_mul_f32_e32 v83, s14, v83
	v_exp_f32_e32 v83, v83
	v_sub_f32_e32 v40, v40, v77
	v_sub_f32_e32 v41, v41, v77
	v_sub_f32_e32 v42, v42, v77
	v_sub_f32_e32 v43, v43, v77
	v_sub_f32_e32 v44, v44, v77
	v_sub_f32_e32 v45, v45, v77
	v_sub_f32_e32 v46, v46, v77
	v_sub_f32_e32 v47, v47, v77
	v_sub_f32_e32 v48, v48, v77
	v_sub_f32_e32 v49, v49, v77
	v_sub_f32_e32 v50, v50, v77
	v_sub_f32_e32 v51, v51, v77
	v_sub_f32_e32 v52, v52, v77
	v_sub_f32_e32 v53, v53, v77
	v_sub_f32_e32 v54, v54, v77
	v_sub_f32_e32 v55, v55, v77
	v_cvt_f64_f32_e32 v[84:85], v83
	v_or_b32_e32 v81, 32, v40
	v_or_b32_e32 v82, 33, v41
	v_min_u32_e32 v80, v81, v82
	v_or_b32_e32 v81, 34, v42
	v_or_b32_e32 v82, 35, v43
	v_min3_u32 v80, v80, v81, v82
	v_or_b32_e32 v81, 36, v44
	v_or_b32_e32 v82, 37, v45
	v_min3_u32 v80, v80, v81, v82
	v_or_b32_e32 v81, 38, v46
	v_or_b32_e32 v82, 39, v47
	v_min3_u32 v80, v80, v81, v82
	v_or_b32_e32 v81, 40, v48
	v_or_b32_e32 v82, 41, v49
	v_min3_u32 v80, v80, v81, v82
	v_or_b32_e32 v81, 42, v50
	v_or_b32_e32 v82, 43, v51
	v_min3_u32 v80, v80, v81, v82
	v_or_b32_e32 v81, 44, v52
	v_or_b32_e32 v82, 45, v53
	v_min3_u32 v80, v80, v81, v82
	v_or_b32_e32 v81, 46, v54
	v_or_b32_e32 v82, 47, v55
	v_min3_u32 v80, v80, v81, v82
	v_mul_f64 v[86:87], v[86:87], v[84:85]
	v_mul_f32_e32 v40, s14, v40
	v_mul_f32_e32 v41, s14, v41
	v_mul_f32_e32 v42, s14, v42
	v_mul_f32_e32 v43, s14, v43
	v_mul_f32_e32 v44, s14, v44
	v_mul_f32_e32 v45, s14, v45
	v_mul_f32_e32 v46, s14, v46
	v_mul_f32_e32 v47, s14, v47
	v_mul_f32_e32 v48, s14, v48
	v_mul_f32_e32 v49, s14, v49
	v_mul_f32_e32 v50, s14, v50
	v_mul_f32_e32 v51, s14, v51
	v_mul_f32_e32 v52, s14, v52
	v_mul_f32_e32 v53, s14, v53
	v_mul_f32_e32 v54, s14, v54
	v_mul_f32_e32 v55, s14, v55
	v_exp_f32_e32 v40, v40
	v_exp_f32_e32 v41, v41
	v_exp_f32_e32 v42, v42
	v_exp_f32_e32 v43, v43
	v_exp_f32_e32 v44, v44
	v_exp_f32_e32 v45, v45
	v_exp_f32_e32 v46, v46
	v_exp_f32_e32 v47, v47
	v_exp_f32_e32 v48, v48
	v_exp_f32_e32 v49, v49
	v_exp_f32_e32 v50, v50
	v_exp_f32_e32 v51, v51
	v_exp_f32_e32 v52, v52
	v_exp_f32_e32 v53, v53
	v_exp_f32_e32 v54, v54
	v_exp_f32_e32 v55, v55
	v_add_f32_e32 v78, v40, v42
	v_add_f32_e32 v79, v41, v43
	v_add_f32_e32 v78, v78, v44
	v_add_f32_e32 v79, v79, v45
	v_add_f32_e32 v78, v78, v46
	v_add_f32_e32 v79, v79, v47
	v_add_f32_e32 v78, v78, v48
	v_add_f32_e32 v79, v79, v49
	v_add_f32_e32 v78, v78, v50
	v_add_f32_e32 v79, v79, v51
	v_add_f32_e32 v78, v78, v52
	v_add_f32_e32 v79, v79, v53
	v_add_f32_e32 v78, v78, v54
	v_add_f32_e32 v79, v79, v55
	v_add_f32_e32 v78, v78, v79
	v_cvt_f64_f32_e32 v[84:85], v78
	v_cndmask_b32_e64 v75, v75, v80, s[20:21]
	v_mov_b32_e32 v73, v77
	v_add_f64 v[86:87], v[86:87], v[84:85]
	s_waitcnt vmcnt(9)
	v_max3_f32 v76, v56, v57, v58
	v_max3_f32 v76, v76, v59, v60
	v_max3_f32 v76, v76, v61, v62
	v_max_f32_e32 v76, v76, v63
	v_max_f32_e32 v77, v73, v76
	v_cmp_gt_f32_e64 s[20:21], v76, v73
	v_sub_f32_e32 v83, v73, v77
	v_mul_f32_e32 v83, s14, v83
	v_exp_f32_e32 v83, v83
	v_sub_f32_e32 v56, v56, v77
	v_sub_f32_e32 v57, v57, v77
	v_sub_f32_e32 v58, v58, v77
	v_sub_f32_e32 v59, v59, v77
	v_sub_f32_e32 v60, v60, v77
	v_sub_f32_e32 v61, v61, v77
	v_sub_f32_e32 v62, v62, v77
	v_sub_f32_e32 v63, v63, v77
	v_cvt_f64_f32_e32 v[84:85], v83
	v_or_b32_e32 v81, 48, v56
	v_or_b32_e32 v82, 49, v57
	v_min_u32_e32 v80, v81, v82
	v_or_b32_e32 v81, 50, v58
	v_or_b32_e32 v82, 51, v59
	v_min3_u32 v80, v80, v81, v82
	v_or_b32_e32 v81, 52, v60
	v_or_b32_e32 v82, 53, v61
	v_min3_u32 v80, v80, v81, v82
	v_or_b32_e32 v81, 54, v62
	v_or_b32_e32 v82, 55, v63
	v_min3_u32 v80, v80, v81, v82
	v_mul_f64 v[86:87], v[86:87], v[84:85]
	v_mul_f32_e32 v56, s14, v56
	v_mul_f32_e32 v57, s14, v57
	v_mul_f32_e32 v58, s14, v58
	v_mul_f32_e32 v59, s14, v59
	v_mul_f32_e32 v60, s14, v60
	v_mul_f32_e32 v61, s14, v61
	v_mul_f32_e32 v62, s14, v62
	v_mul_f32_e32 v63, s14, v63
	v_exp_f32_e32 v56, v56
	v_exp_f32_e32 v57, v57
	v_exp_f32_e32 v58, v58
	v_exp_f32_e32 v59, v59
	v_exp_f32_e32 v60, v60
	v_exp_f32_e32 v61, v61
	v_exp_f32_e32 v62, v62
	v_exp_f32_e32 v63, v63
	v_add_f32_e32 v78, v56, v58
	v_add_f32_e32 v79, v57, v59
	v_add_f32_e32 v78, v78, v60
	v_add_f32_e32 v79, v79, v61
	v_add_f32_e32 v78, v78, v62
	v_add_f32_e32 v79, v79, v63
	v_add_f32_e32 v78, v78, v79
	v_cvt_f64_f32_e32 v[84:85], v78
	v_cndmask_b32_e64 v75, v75, v80, s[20:21]
	v_mov_b32_e32 v73, v77
	v_add_f64 v[86:87], v[86:87], v[84:85]
	s_waitcnt vmcnt(4)
	v_max3_f32 v76, v64, v65, v66
	v_max3_f32 v76, v76, v67, v68
	v_max_f32_e32 v77, v73, v76
	v_cmp_gt_f32_e64 s[20:21], v76, v73
	v_sub_f32_e32 v83, v73, v77
	v_mul_f32_e32 v83, s14, v83
	v_exp_f32_e32 v83, v83
	v_sub_f32_e32 v64, v64, v77
	v_sub_f32_e32 v65, v65, v77
	v_sub_f32_e32 v66, v66, v77
	v_sub_f32_e32 v67, v67, v77
	v_sub_f32_e32 v68, v68, v77
	v_cvt_f64_f32_e32 v[84:85], v83
	v_or_b32_e32 v81, 56, v64
	v_or_b32_e32 v82, 57, v65
	v_min_u32_e32 v80, v81, v82
	v_or_b32_e32 v81, 58, v66
	v_or_b32_e32 v82, 59, v67
	v_min3_u32 v80, v80, v81, v82
	v_or_b32_e32 v81, 60, v68
	v_min_u32_e32 v80, v80, v81
	v_mul_f64 v[86:87], v[86:87], v[84:85]
	v_mul_f32_e32 v64, s14, v64
	v_mul_f32_e32 v65, s14, v65
	v_mul_f32_e32 v66, s14, v66
	v_mul_f32_e32 v67, s14, v67
	v_mul_f32_e32 v68, s14, v68
	v_exp_f32_e32 v64, v64
	v_exp_f32_e32 v65, v65
	v_exp_f32_e32 v66, v66
	v_exp_f32_e32 v67, v67
	v_exp_f32_e32 v68, v68
	v_add_f32_e32 v78, v64, v66
	v_add_f32_e32 v79, v65, v67
	v_add_f32_e32 v78, v78, v68
	v_add_f32_e32 v78, v78, v79
	v_cvt_f64_f32_e32 v[84:85], v78
	v_cndmask_b32_e64 v75, v75, v80, s[20:21]
	v_mov_b32_e32 v73, v77
	v_add_f64 v[86:87], v[86:87], v[84:85]
	s_waitcnt vmcnt(1)
	v_max3_f32 v76, v69, v70, v71
	v_max_f32_e32 v77, v73, v76
	v_cmp_gt_f32_e64 s[20:21], v76, v73
	v_sub_f32_e32 v83, v73, v77
	v_mul_f32_e32 v83, s14, v83
	v_exp_f32_e32 v83, v83
	v_sub_f32_e32 v69, v69, v77
	v_sub_f32_e32 v70, v70, v77
	v_sub_f32_e32 v71, v71, v77
	v_cvt_f64_f32_e32 v[84:85], v83
	v_or_b32_e32 v81, 61, v69
	v_or_b32_e32 v82, 62, v70
	v_min_u32_e32 v80, v81, v82
	v_or_b32_e32 v81, 63, v71
	v_min_u32_e32 v80, v80, v81
	v_mul_f64 v[86:87], v[86:87], v[84:85]
	v_mul_f32_e32 v69, s14, v69
	v_mul_f32_e32 v70, s14, v70
	v_mul_f32_e32 v71, s14, v71
	v_exp_f32_e32 v69, v69
	v_exp_f32_e32 v70, v70
	v_exp_f32_e32 v71, v71
	v_add_f32_e32 v78, v69, v70
	v_add_f32_e32 v78, v78, v71
	v_cvt_f64_f32_e32 v[84:85], v78
	v_cndmask_b32_e64 v75, v75, v80, s[20:21]
	v_mov_b32_e32 v73, v77
	v_add_f64 v[86:87], v[86:87], v[84:85]
	s_waitcnt vmcnt(0)
	v_max_f32_e32 v77, v73, v72
	v_cmp_gt_f32_e64 s[20:21], v72, v73
	v_sub_f32_e32 v83, v73, v77
	v_sub_f32_e32 v72, v72, v77
	v_mul_f32_e32 v83, s14, v83
	v_mul_f32_e32 v72, s14, v72
	v_exp_f32_e32 v83, v83
	v_exp_f32_e32 v72, v72
	v_cndmask_b32_e64 v75, v75, 64, s[20:21]
	v_cvt_f64_f32_e32 v[84:85], v83
	v_cvt_f64_f32_e32 v[90:91], v72
	v_mul_f64 v[86:87], v[86:87], v[84:85]
	v_add_f64 v[86:87], v[86:87], v[90:91]
	v_rcp_f64_e32 v[88:89], v[86:87]
	v_cmp_gt_u32_e32 vcc, 64, v75
	s_and_b64 vcc, vcc, s[36:37]
	v_fma_f64 v[90:91], -v[86:87], v[88:89], 1.0
	v_fma_f64 v[88:89], v[90:91], v[88:89], v[88:89]
	v_cvt_f32_f64_e32 v3, v[88:89]
	v_cndmask_b32_e32 v74, 0, v3, vcc
	global_store_dwordx2 v98, v[74:75], s[6:7]
